# router phase: next 512-column chunk of x1 prefetched into dead registers under the current chunk's f32 MFMAs (was one exposed round trip per chunk)
# baseline (speedup 1.0000x reference)
; __device__ __forceinline__ void ph12_body(const Args& a, LAS unsigned char* lds, int tid, int wave, int lane, int G, int bid, size_t alt) {
;     ...
;         const int t0 = tile * 32, b = t0 >> 11; const int lrow = tid >> 4, cg = tid & 15;
;         f32x16 acc;
; #pragma unroll
;         for (int i = 0; i < 16; ++i) acc[i] = 0.f;
;         float ss = 0.f;
;         if (tid < 32) lcnt[tid] = 0u;
;         for (int ch = 0; ch < 4; ++ch) {
;             f32x4 v[8]; const v2u* xr = (const v2u*)(X1 + (size_t)(t0 + lrow) * DM + ch * 512) + cg;
; #pragma unroll
;             for (int j = 0; j < 8; ++j) { const v2u w = xr[16 * j]; v[j] = (f32x4){bflo(w.x), bfhi(w.x), bflo(w.y), bfhi(w.y)}; ss += (v[j][0] * v[j][0] + v[j][1] * v[j][1]) + (v[j][2] * v[j][2] + v[j][3] * v[j][3]); }
;             float wv[32]; const float* wp = WRP + (size_t)b * (DM * NEXP) + (size_t)(ch * 512 + 64 * wave + (lane >> 5)) * NEXP + (lane & 31);
; #pragma unroll
;             for (int q = 0; q < 32; ++q) wv[q] = wp[2 * q * NEXP];
;             __syncthreads();
; #pragma unroll
;             for (int j = 0; j < 8; ++j)
; #pragma unroll
;                 for (int e = 0; e < 4; ++e) xs[lrow * 513 + cg * 4 + 64 * j + e] = v[j][e];
;             __syncthreads();
.LBB0_1088:
	s_and_saveexec_b64 s[70:71], s[0:1]
	ds_write_b32 v179, v155
	s_or_b64 exec, exec, s[70:71]
	s_ashr_i32 s86, s2, 6
	v_ashrrev_i32_e32 v173, 31, v172
	s_ashr_i32 s87, s86, 31
	v_lshlrev_b64 v[2:3], 12, v[172:173]
	s_lshl_b64 s[70:71], s[86:87], 18
	v_mov_b32_e32 v24, 0
	v_lshl_add_u64 v[18:19], v[170:171], 0, v[2:3]
	v_lshl_add_u64 v[20:21], v[156:157], 0, s[70:71]
	s_mov_b64 s[70:71], 0
	v_mov_b32_e32 v22, v211
	v_mov_b32_e32 v2, 0
	v_mov_b32_e32 v3, v24
	v_mov_b32_e32 v4, v24
	v_mov_b32_e32 v5, v24
	v_mov_b32_e32 v6, v24
	v_mov_b32_e32 v7, v24
	v_mov_b32_e32 v8, v24
	v_mov_b32_e32 v9, v24
	v_mov_b32_e32 v10, v24
	v_mov_b32_e32 v11, v24
	v_mov_b32_e32 v12, v24
	v_mov_b32_e32 v13, v24
	v_mov_b32_e32 v14, v24
	v_mov_b32_e32 v15, v24
	v_mov_b32_e32 v16, v24
	v_mov_b32_e32 v17, v24
	s_mov_b32 s98, 0xf100000
	s_mov_b32 s99, 0
	v_lshl_add_u64 v[248:249], v[18:19], 0, s[98:99]
	global_load_dwordx2 v[232:233], v[248:249], off
	global_load_dwordx2 v[234:235], v[248:249], off offset:128
	global_load_dwordx2 v[236:237], v[248:249], off offset:256
	global_load_dwordx2 v[238:239], v[248:249], off offset:384
	global_load_dwordx2 v[240:241], v[248:249], off offset:512
	global_load_dwordx2 v[242:243], v[248:249], off offset:640
	global_load_dwordx2 v[244:245], v[248:249], off offset:768
	global_load_dwordx2 v[246:247], v[248:249], off offset:896
.LBB0_1091:
	v_lshl_add_u64 v[26:27], v[18:19], 0, s[70:71]
	s_mov_b32 s82, 0xf100000
	v_add_co_u32_e32 v26, vcc, s82, v26
	v_ashrrev_i32_e32 v23, 31, v22
	s_nop 0
	v_addc_co_u32_e32 v27, vcc, 0, v27, vcc
	s_waitcnt lgkmcnt(0)
	s_nop 0
	s_movk_i32 s98, 0x400
	s_mov_b32 s99, 0
	v_lshl_add_u64 v[248:249], v[26:27], 0, s[98:99]
	v_lshlrev_b64 v[28:29], 7, v[22:23]
	v_lshl_add_u64 v[28:29], v[20:21], 0, v[28:29]
	global_load_dword v23, v[28:29], off
	global_load_dword v57, v[28:29], off offset:256
	global_load_dword v58, v[28:29], off offset:512
	global_load_dword v59, v[28:29], off offset:768
	global_load_dword v60, v[28:29], off offset:1024
	global_load_dword v61, v[28:29], off offset:1280
	global_load_dword v62, v[28:29], off offset:1536
	global_load_dword v63, v[28:29], off offset:1792
	global_load_dword v64, v[28:29], off offset:2048
	global_load_dword v65, v[28:29], off offset:2304
	global_load_dword v66, v[28:29], off offset:2560
	global_load_dword v67, v[28:29], off offset:2816
	global_load_dword v68, v[28:29], off offset:3072
	global_load_dword v69, v[28:29], off offset:3328
	global_load_dword v70, v[28:29], off offset:3584
	global_load_dword v71, v[28:29], off offset:3840
	s_movk_i32 s82, 0x1000
	v_add_co_u32_e32 v28, vcc, s82, v28
	v_add_u32_e32 v52, 0x508, v212
	s_nop 0
	v_addc_co_u32_e32 v29, vcc, 0, v29, vcc
	v_add_u32_e32 v53, 0x600, v212
	global_load_dword v72, v[28:29], off
	global_load_dword v73, v[28:29], off offset:256
	global_load_dword v74, v[28:29], off offset:512
	global_load_dword v75, v[28:29], off offset:768
	global_load_dword v76, v[28:29], off offset:1024
	global_load_dword v77, v[28:29], off offset:1280
	global_load_dword v78, v[28:29], off offset:1536
	global_load_dword v79, v[28:29], off offset:1792
	global_load_dword v80, v[28:29], off offset:2048
	global_load_dword v81, v[28:29], off offset:2304
	global_load_dword v82, v[28:29], off offset:2560
	global_load_dword v83, v[28:29], off offset:2816
	global_load_dword v84, v[28:29], off offset:3072
	global_load_dword v85, v[28:29], off offset:3328
	global_load_dword v86, v[28:29], off offset:3584
	global_load_dword v87, v[28:29], off offset:3840
	v_add_u32_e32 v25, 0x400, v212
	v_add_u32_e32 v44, 0x408, v212
	v_add_u32_e32 v50, 0x500, v212
	v_add_u32_e32 v54, 0x608, v212
	v_add_u32_e32 v55, 0x700, v212
	v_add_u32_e32 v56, 0x708, v212
	s_barrier
	s_add_u32 s70, s70, 0x400
	s_addc_u32 s71, s71, 0
	v_add_u32_e32 v22, 0x200, v22
	s_cmpk_eq_i32 s70, 0x1000
	s_waitcnt vmcnt(32)
	v_mov_b32_e32 v30, v232
	v_mov_b32_e32 v31, v233
	v_mov_b32_e32 v32, v234
	v_mov_b32_e32 v33, v235
	v_mov_b32_e32 v34, v236
	v_mov_b32_e32 v35, v237
	v_mov_b32_e32 v36, v238
	v_mov_b32_e32 v37, v239
	v_mov_b32_e32 v38, v240
	v_mov_b32_e32 v39, v241
	v_mov_b32_e32 v40, v242
	v_mov_b32_e32 v41, v243
	v_mov_b32_e32 v42, v244
	v_mov_b32_e32 v43, v245
	v_mov_b32_e32 v26, v246
	v_mov_b32_e32 v27, v247
	global_load_dwordx2 v[232:233], v[248:249], off
	global_load_dwordx2 v[234:235], v[248:249], off offset:128
	global_load_dwordx2 v[236:237], v[248:249], off offset:256
	global_load_dwordx2 v[238:239], v[248:249], off offset:384
	global_load_dwordx2 v[240:241], v[248:249], off offset:512
	global_load_dwordx2 v[242:243], v[248:249], off offset:640
	global_load_dwordx2 v[244:245], v[248:249], off offset:768
	global_load_dwordx2 v[246:247], v[248:249], off offset:896
	v_lshlrev_b32_e32 v28, 16, v30
	v_and_b32_e32 v30, 0xffff0000, v30
	v_lshlrev_b32_e32 v29, 16, v31
	v_and_b32_e32 v31, 0xffff0000, v31
	v_lshlrev_b32_e32 v88, 16, v32
	v_and_b32_e32 v89, 0xffff0000, v32
	v_lshlrev_b32_e32 v32, 16, v33
	v_and_b32_e32 v33, 0xffff0000, v33
	v_lshlrev_b32_e32 v45, 16, v34
	v_and_b32_e32 v90, 0xffff0000, v34
	v_lshlrev_b32_e32 v91, 16, v35
	v_and_b32_e32 v92, 0xffff0000, v35
	v_lshlrev_b32_e32 v35, 16, v37
	v_lshlrev_b32_e32 v34, 16, v36
	v_and_b32_e32 v37, 0xffff0000, v37
	v_and_b32_e32 v36, 0xffff0000, v36
	v_lshlrev_b32_e32 v47, 16, v39
	v_lshlrev_b32_e32 v46, 16, v38
	v_and_b32_e32 v39, 0xffff0000, v39
	v_and_b32_e32 v38, 0xffff0000, v38
	v_lshlrev_b32_e32 v48, 16, v40
	v_and_b32_e32 v49, 0xffff0000, v40
	v_lshlrev_b32_e32 v40, 16, v41
	v_and_b32_e32 v41, 0xffff0000, v41
	v_lshlrev_b32_e32 v51, 16, v42
	v_and_b32_e32 v93, 0xffff0000, v42
	v_lshlrev_b32_e32 v94, 16, v43
	v_and_b32_e32 v95, 0xffff0000, v43
	v_lshlrev_b32_e32 v43, 16, v27
	v_lshlrev_b32_e32 v42, 16, v26
	v_and_b32_e32 v27, 0xffff0000, v27
	v_and_b32_e32 v26, 0xffff0000, v26
	ds_write2_b32 v212, v28, v30 offset1:1
	ds_write2_b32 v212, v29, v31 offset0:2 offset1:3
	ds_write2_b32 v212, v88, v89 offset0:64 offset1:65
	ds_write2_b32 v212, v32, v33 offset0:66 offset1:67
	ds_write2_b32 v212, v45, v90 offset0:128 offset1:129
	ds_write2_b32 v212, v91, v92 offset0:130 offset1:131
	ds_write2_b32 v212, v34, v36 offset0:192 offset1:193
	ds_write2_b32 v212, v35, v37 offset0:194 offset1:195
	ds_write2_b32 v25, v46, v38 offset1:1
	ds_write2_b32 v44, v47, v39 offset1:1
	ds_write2_b32 v50, v48, v49 offset1:1
	ds_write2_b32 v52, v40, v41 offset1:1
	ds_write2_b32 v53, v51, v93 offset1:1
	ds_write2_b32 v54, v94, v95 offset1:1
	ds_write2_b32 v55, v42, v26 offset1:1
	ds_write2_b32 v56, v43, v27 offset1:1
	s_waitcnt lgkmcnt(0)
	s_barrier
; #define LAS __attribute__((address_space(3)))
; __device__ __forceinline__ void ph12_body(const Args& a, LAS unsigned char* lds, int tid, int wave, int lane, int G, int bid, size_t alt) {
;     ...
;             for (int j = 0; j < 8; ++j) { const v2u w = xr[16 * j]; v[j] = (f32x4){bflo(w.x), bfhi(w.x), bflo(w.y), bfhi(w.y)}; ss += (v[j][0] * v[j][0] + v[j][1] * v[j][1]) + (v[j][2] * v[j][2] + v[j][3] * v[j][3]); }
;     ...
;             const LAS float* xq = xs + (lane & 31) * 513 + 64 * wave + (lane >> 5);
; #pragma unroll
;             for (int q = 0; q < 32; ++q) acc = __builtin_amdgcn_mfma_f32_32x32x2f32(xq[2 * q], wv[q], acc, 0, 0, 0);
	ds_read2_b32 v[52:53], v193 offset1:2
	s_waitcnt vmcnt(39) lgkmcnt(0)
	v_mfma_f32_32x32x2_f32 v[2:17], v52, v23, v[2:17]
	ds_read2_b32 v[54:55], v193 offset0:60 offset1:62
	v_mul_f32_e64 v30, v30, v30
	v_mul_f32_e64 v31, v31, v31
	v_mul_f32_e32 v44, v88, v88
	v_mul_f32_e64 v36, v36, v36
	v_mul_f32_e64 v37, v37, v37
	v_mul_f32_e64 v38, v38, v38
	v_mul_f32_e64 v39, v39, v39
	v_mul_f32_e32 v50, v33, v33
	v_fma_f32 v28, v28, v28, v30
	v_fma_f32 v29, v29, v29, v31
	v_mul_f32_e32 v23, v90, v90
	v_mul_f32_e64 v26, v26, v26
	v_mul_f32_e64 v27, v27, v27
	v_pk_fma_f32 v[30:31], v[34:35], v[34:35], v[36:37]
	v_pk_fma_f32 v[34:35], v[46:47], v[46:47], v[38:39]
	v_pk_mul_f32 v[38:39], v[44:45], v[44:45]
	v_pk_fma_f32 v[32:33], v[32:33], v[32:33], v[50:51] op_sel_hi:[1,1,0]
	v_pk_add_f32 v[28:29], v[28:29], v[28:29] op_sel:[0,1] op_sel_hi:[1,0]
	v_mul_f32_e32 v25, v91, v91
	s_waitcnt vmcnt(38)
	v_mfma_f32_32x32x2_f32 v[2:17], v53, v57, v[2:17]
	ds_read2_b32 v[52:53], v193 offset0:4 offset1:6
	v_fma_f32 v26, v42, v42, v26
	v_fma_f32 v27, v43, v43, v27
	v_mov_b32_e32 v33, v23
	v_add_f32_e32 v23, v26, v27
	v_mul_f32_e32 v56, v49, v49
	v_mov_b32_e32 v57, v51
	v_pk_add_f32 v[30:31], v[30:31], v[30:31] op_sel:[0,1] op_sel_hi:[1,0]
	v_pk_fma_f32 v[42:43], v[48:49], v[48:49], v[56:57] op_sel_hi:[1,1,0]
	v_mov_b32_e32 v56, v30
	v_pk_add_f32 v[34:35], v[34:35], v[34:35] op_sel:[0,1] op_sel_hi:[1,0]
	s_waitcnt vmcnt(37) lgkmcnt(0)
	v_mfma_f32_32x32x2_f32 v[2:17], v52, v58, v[2:17]
	v_mul_f32_e32 v58, v41, v41
	s_waitcnt vmcnt(36)
	v_mfma_f32_32x32x2_f32 v[2:17], v53, v59, v[2:17]
	ds_read2_b32 v[52:53], v193 offset0:8 offset1:10
	v_mul_f32_e32 v59, v92, v92
	v_mov_b32_e32 v29, v59
	v_add_f32_e64 v24, v24, v28
	v_add_f32_e64 v25, v25, v29
	v_fma_f32 v40, v40, v40, v58
	v_fma_f32 v41, v41, v41, v58
	s_waitcnt vmcnt(35) lgkmcnt(0)
	v_mfma_f32_32x32x2_f32 v[2:17], v52, v60, v[2:17]
	v_mul_f32_e32 v60, v93, v93
	v_mov_b32_e32 v35, v60
	s_waitcnt vmcnt(34)
	v_mfma_f32_32x32x2_f32 v[2:17], v53, v61, v[2:17]
	ds_read2_b32 v[52:53], v193 offset0:12 offset1:14
	v_mul_f32_e32 v61, v94, v94
	v_mov_b32_e32 v43, v61
	s_waitcnt vmcnt(33) lgkmcnt(0)
	v_mfma_f32_32x32x2_f32 v[2:17], v52, v62, v[2:17]
	v_mul_f32_e32 v62, v95, v95
	v_mov_b32_e32 v41, v62
	s_waitcnt vmcnt(32)
	v_mfma_f32_32x32x2_f32 v[2:17], v53, v63, v[2:17]
	ds_read2_b32 v[52:53], v193 offset0:16 offset1:18
	s_waitcnt vmcnt(31) lgkmcnt(0)
	v_mfma_f32_32x32x2_f32 v[2:17], v52, v64, v[2:17]
	s_waitcnt vmcnt(30)
	v_mfma_f32_32x32x2_f32 v[2:17], v53, v65, v[2:17]
	ds_read2_b32 v[52:53], v193 offset0:20 offset1:22
	s_waitcnt vmcnt(29) lgkmcnt(0)
	v_mfma_f32_32x32x2_f32 v[2:17], v52, v66, v[2:17]
	s_waitcnt vmcnt(28)
	v_mfma_f32_32x32x2_f32 v[2:17], v53, v67, v[2:17]
	ds_read2_b32 v[52:53], v193 offset0:24 offset1:26
	s_waitcnt vmcnt(27) lgkmcnt(0)
	v_mfma_f32_32x32x2_f32 v[2:17], v52, v68, v[2:17]
	s_waitcnt vmcnt(26)
	v_mfma_f32_32x32x2_f32 v[2:17], v53, v69, v[2:17]
	ds_read2_b32 v[52:53], v193 offset0:28 offset1:30
	s_waitcnt vmcnt(25) lgkmcnt(0)
	v_mfma_f32_32x32x2_f32 v[2:17], v52, v70, v[2:17]
	s_waitcnt vmcnt(24)
	v_mfma_f32_32x32x2_f32 v[2:17], v53, v71, v[2:17]
	ds_read2_b32 v[52:53], v193 offset0:32 offset1:34
	s_waitcnt vmcnt(23) lgkmcnt(0)
	v_mfma_f32_32x32x2_f32 v[2:17], v52, v72, v[2:17]
	s_waitcnt vmcnt(22)
	v_mfma_f32_32x32x2_f32 v[2:17], v53, v73, v[2:17]
	ds_read2_b32 v[52:53], v193 offset0:36 offset1:38
	s_waitcnt vmcnt(21) lgkmcnt(0)
	v_mfma_f32_32x32x2_f32 v[2:17], v52, v74, v[2:17]
	s_waitcnt vmcnt(20)
	v_mfma_f32_32x32x2_f32 v[2:17], v53, v75, v[2:17]
	ds_read2_b32 v[52:53], v193 offset0:40 offset1:42
	s_waitcnt vmcnt(19) lgkmcnt(0)
	v_mfma_f32_32x32x2_f32 v[2:17], v52, v76, v[2:17]
	s_waitcnt vmcnt(18)
	v_mfma_f32_32x32x2_f32 v[2:17], v53, v77, v[2:17]
	ds_read2_b32 v[52:53], v193 offset0:44 offset1:46
	s_waitcnt vmcnt(17) lgkmcnt(0)
	v_mfma_f32_32x32x2_f32 v[2:17], v52, v78, v[2:17]
	s_waitcnt vmcnt(16)
	v_mfma_f32_32x32x2_f32 v[2:17], v53, v79, v[2:17]
	ds_read2_b32 v[52:53], v193 offset0:48 offset1:50
	s_waitcnt vmcnt(15) lgkmcnt(0)
	v_mfma_f32_32x32x2_f32 v[2:17], v52, v80, v[2:17]
	s_waitcnt vmcnt(14)
	v_mfma_f32_32x32x2_f32 v[2:17], v53, v81, v[2:17]
	ds_read2_b32 v[52:53], v193 offset0:52 offset1:54
	s_waitcnt vmcnt(13) lgkmcnt(0)
	v_mfma_f32_32x32x2_f32 v[2:17], v52, v82, v[2:17]
	s_waitcnt vmcnt(12)
	v_mfma_f32_32x32x2_f32 v[2:17], v53, v83, v[2:17]
	ds_read2_b32 v[52:53], v193 offset0:56 offset1:58
	s_waitcnt vmcnt(11) lgkmcnt(0)
	v_mfma_f32_32x32x2_f32 v[2:17], v52, v84, v[2:17]
	v_mul_f32_e32 v52, v89, v89
	s_waitcnt vmcnt(10)
	v_mfma_f32_32x32x2_f32 v[2:17], v53, v85, v[2:17]
	v_mov_b32_e32 v53, v45
	v_add_f32_e64 v36, v44, v52
	v_add_f32_e64 v37, v45, v53
	v_mov_b32_e32 v37, v39
	v_add_f32_e64 v26, v36, v32
	v_add_f32_e64 v27, v37, v33
	v_add_f32_e64 v32, v42, v40
	v_add_f32_e64 v33, v43, v41
	v_add_f32_e64 v24, v26, v24
	v_add_f32_e64 v25, v27, v25
	v_pk_add_f32 v[24:25], v[24:25], v[24:25] op_sel:[0,1] op_sel_hi:[1,0]
	s_nop 0
	v_mov_b32_e32 v50, v24
	v_pk_add_f32 v[24:25], v[24:25], v[30:31]
	v_pk_mul_f32 v[26:27], v[50:51], v[56:57]
	s_nop 0
	v_mov_b32_e32 v25, v27
	s_waitcnt vmcnt(9)
	v_mfma_f32_32x32x2_f32 v[2:17], v54, v86, v[2:17]
	v_add_f32_e64 v24, v24, v34
	v_add_f32_e64 v25, v25, v35
	v_add_f32_e64 v24, v24, v32
	v_add_f32_e64 v25, v25, v33
	v_add_f32_e32 v24, v24, v25
	v_add_f32_e32 v24, v24, v23
	s_waitcnt vmcnt(8)
	v_mfma_f32_32x32x2_f32 v[2:17], v55, v87, v[2:17]
	s_cbranch_scc0 .LBB0_1091
; __device__ __forceinline__ void ph12_body(const Args& a, LAS unsigned char* lds, int tid, int wave, int lane, int G, int bid, size_t alt) {
;     ...
;         ss += __shfl_xor(ss, 1); ss += __shfl_xor(ss, 2); ss += __shfl_xor(ss, 4); ss += __shfl_xor(ss, 8);
;         if (cg == 0) { const float rstd = 1.0f / sqrtf(ss * (1.0f / DM) + RMS_EPS); rstdL[lrow] = rstd; RSTD[t0 + lrow] = rstd; }
	ds_bpermute_b32 v18, v207, v24
	s_lshl_b32 s82, s2, 5
	s_waitcnt lgkmcnt(0)
	v_add_f32_e32 v18, v24, v18
	ds_bpermute_b32 v19, v208, v18
	s_waitcnt lgkmcnt(0)
	v_add_f32_e32 v18, v18, v19
	ds_bpermute_b32 v19, v209, v18
	s_waitcnt lgkmcnt(0)
	v_add_f32_e32 v18, v18, v19
	ds_bpermute_b32 v19, v210, v18
	s_mov_b64 s[88:89], exec
	v_readlane_b32 s70, v250, 55
	v_readlane_b32 s71, v250, 56
	s_and_b64 s[70:71], s[88:89], s[70:71]
	s_mov_b64 exec, s[70:71]
	s_cbranch_execz .LBB0_1094
	s_waitcnt lgkmcnt(0)
	v_add_f32_e32 v18, v18, v19
	v_fmamk_f32 v18, v18, 0x3a000000, v213
	s_mov_b32 s70, 0xf800000
	v_mul_f32_e32 v19, 0x4f800000, v18
	v_cmp_gt_f32_e32 vcc, s70, v18
	s_nop 1
	v_cndmask_b32_e32 v18, v18, v19, vcc
	v_sqrt_f32_e32 v19, v18
	s_nop 0
	v_add_u32_e32 v20, -1, v19
	v_fma_f32 v22, -v20, v19, v18
	v_add_u32_e32 v21, 1, v19
	v_cmp_ge_f32_e64 s[70:71], 0, v22
	s_nop 1
	v_cndmask_b32_e64 v20, v19, v20, s[70:71]
	v_fma_f32 v19, -v21, v19, v18
	v_cmp_lt_f32_e64 s[70:71], 0, v19
	s_nop 1
	v_cndmask_b32_e64 v19, v20, v21, s[70:71]
	v_mul_f32_e32 v20, 0x37800000, v19
	v_cndmask_b32_e32 v19, v19, v20, vcc
	v_cmp_class_f32_e32 vcc, v18, v214
	s_nop 1
	v_cndmask_b32_e32 v20, v19, v18, vcc
	v_div_scale_f32 v21, s[70:71], v20, v20, 1.0
	v_rcp_f32_e32 v22, v21
	v_add_u32_e32 v18, s82, v1
	v_readlane_b32 s70, v251, 27
	v_ashrrev_i32_e32 v19, 31, v18
	v_fma_f32 v23, -v21, v22, 1.0
	v_fmac_f32_e32 v22, v23, v22
	v_div_scale_f32 v23, vcc, 1.0, v20, 1.0
	v_mul_f32_e32 v24, v23, v22
	v_fma_f32 v25, -v21, v24, v23
	v_fmac_f32_e32 v24, v25, v22
	v_fma_f32 v21, -v21, v24, v23
	v_div_fmas_f32 v21, v21, v22, v24
	v_readlane_b32 s71, v251, 28
	v_div_fixup_f32 v20, v21, v20, 1.0
	ds_write_b32 v194, v20
	v_lshl_add_u64 v[18:19], v[18:19], 2, s[70:71]
	global_store_dword v[18:19], v20, off
